# fused differential attention v3: LDS fragment reads issued early (before LDS-DMA issue / softmax); same math
# speedup vs baseline: 1.1029x; 1.0024x over previous
.Lfa_entry:
	s_waitcnt lgkmcnt(0)
	s_load_dwordx2 s[0:1], s[30:31], 0xd8
	v_mbcnt_lo_u32_b32 v0, -1, 0
	v_mbcnt_hi_u32_b32 v0, -1, v0
	s_lshr_b32 s15, s3, 6
	s_lshl_b32 s20, s15, 10
	s_mul_i32 s21, s15, 0xc00
	s_add_i32 s21, s21, 0x18800
	v_lshlrev_b32_e32 v1, 2, v0
	v_add_u32_e32 v1, s21, v1
	ds_write_b32 v1, v162 offset:0
	ds_write_b32 v1, v163 offset:256
	ds_write_b32 v1, v164 offset:512
	ds_write_b32 v1, v165 offset:768
	ds_write_b32 v1, v166 offset:1024
	ds_write_b32 v1, v167 offset:1280
	ds_write_b32 v1, v168 offset:1536
	ds_write_b32 v1, v169 offset:1792
	ds_write_b32 v1, v170 offset:2048
	ds_write_b32 v1, v171 offset:2304
	ds_write_b32 v1, v172 offset:2560
	ds_write_b32 v1, v173 offset:2816
	v_and_b32_e32 v2, 31, v0
	v_lshrrev_b32_e32 v3, 5, v0
	v_lshlrev_b32_e32 v208, 8, v2
	v_and_b32_e32 v4, 7, v2
	v_lshlrev_b32_e32 v4, 4, v4
	v_lshlrev_b32_e32 v5, 4, v3
	v_xor_b32_e32 v209, v4, v5
	v_and_b32_e32 v4, 3, v0
	v_lshlrev_b32_e32 v4, 3, v4
	v_bfe_u32 v5, v0, 2, 2
	v_lshl_or_b32 v4, v5, 6, v4
	v_bfe_u32 v5, v0, 4, 1
	v_lshl_or_b32 v4, v5, 5, v4
	v_lshl_or_b32 v210, v3, 8, v4
	s_add_i32 s21, s20, 0x1e800
	v_lshl_add_u32 v11, v0, 2, s21
	v_lshrrev_b32_e32 v4, 4, v0
	v_and_b32_e32 v5, 15, v0
	s_add_i32 s21, s15, 0
	s_lshl_b32 s21, s21, 2
	v_add_u32_e32 v6, s21, v4
	v_and_b32_e32 v7, 7, v6
	v_xor_b32_e32 v7, v5, v7
	v_lshlrev_b32_e32 v7, 4, v7
	v_lshl_or_b32 v12, v6, 8, v7
	ds_write_b32 v11, v12 offset:0
	s_add_i32 s21, s15, 8
	s_lshl_b32 s21, s21, 2
	v_add_u32_e32 v6, s21, v4
	v_and_b32_e32 v7, 7, v6
	v_xor_b32_e32 v7, v5, v7
	v_lshlrev_b32_e32 v7, 4, v7
	v_lshl_or_b32 v12, v6, 8, v7
	ds_write_b32 v11, v12 offset:256
	v_bfe_u32 v4, v0, 2, 3
	v_and_b32_e32 v5, 3, v0
	v_lshlrev_b32_e32 v5, 4, v5
	s_add_i32 s21, s15, 0
	s_lshl_b32 s21, s21, 1
	v_add_u32_e32 v6, s21, v3
	v_lshrrev_b32_e32 v7, 2, v6
	v_lshl_or_b32 v7, v7, 3, v4
	v_and_b32_e32 v8, 3, v6
	v_lshl_or_b32 v8, v8, 6, v5
	v_and_b32_e32 v9, 0xfffffff3, v7
	v_bfe_u32 v10, v7, 2, 1
	v_lshl_or_b32 v9, v10, 3, v9
	v_bfe_u32 v10, v7, 3, 1
	v_lshl_or_b32 v9, v10, 2, v9
	v_lshl_or_b32 v12, v9, 8, v8
	ds_write_b32 v11, v12 offset:512
	s_add_i32 s21, s15, 8
	s_lshl_b32 s21, s21, 1
	v_add_u32_e32 v6, s21, v3
	v_lshrrev_b32_e32 v7, 2, v6
	v_lshl_or_b32 v7, v7, 3, v4
	v_and_b32_e32 v8, 3, v6
	v_lshl_or_b32 v8, v8, 6, v5
	v_and_b32_e32 v9, 0xfffffff3, v7
	v_bfe_u32 v10, v7, 2, 1
	v_lshl_or_b32 v9, v10, 3, v9
	v_bfe_u32 v10, v7, 3, 1
	v_lshl_or_b32 v9, v10, 2, v9
	v_lshl_or_b32 v12, v9, 8, v8
	ds_write_b32 v11, v12 offset:768
	s_waitcnt lgkmcnt(0)
	s_mov_b32 s2, s94
.Lfa_task:
	s_cmpk_lt_u32 s2, 0x100
	s_cbranch_scc0 .Lfa_done
	s_and_b32 s21, s2, 7
	s_lshr_b32 s74, s2, 3
	s_lshr_b32 s10, s74, 3
	s_lshl_b32 s21, s21, 2
	s_add_i32 s10, s10, s21
	s_and_b32 s74, s74, 7
	s_lshl_b32 s89, s74, 1
	s_mov_b32 s9, 0
.Lfa_block:
	s_lshr_b32 s21, s9, 1
	s_add_i32 s8, s89, s21
	s_sub_i32 s21, 31, s8
	s_bitcmp1_b32 s9, 0
	s_cselect_b32 s8, s21, s8
	s_lshl_b32 s21, s10, 21
	s_add_u32 s28, s0, 0x402ac000
	s_addc_u32 s29, s1, 0
	s_add_u32 s28, s28, s21
	s_addc_u32 s29, s29, 0
	s_lshr_b32 s74, s10, 1
	s_lshl_b32 s74, s74, 22
	s_add_u32 s34, s0, 0x442ac000
	s_addc_u32 s35, s1, 0
	s_add_u32 s34, s34, s74
	s_addc_u32 s35, s35, 0
	s_add_u32 s38, s34, 0x200000
	s_addc_u32 s39, s35, 0
	s_lshl_b32 s74, s8, 16
	s_add_u32 s40, s0, 0x482ac000
	s_addc_u32 s41, s1, 0
	s_add_u32 s40, s40, s21
	s_addc_u32 s41, s41, 0
	s_add_u32 s40, s40, s74
	s_addc_u32 s41, s41, 0
	s_lshl_b32 s21, s10, 22
	s_add_u32 s42, s0, 0x382ac000
	s_addc_u32 s43, s1, 0
	s_add_u32 s42, s42, s21
	s_addc_u32 s43, s43, 0
	s_add_u32 s42, s42, s74
	s_addc_u32 s43, s43, 0
	s_add_u32 s44, s42, 0x200000
	s_addc_u32 s45, s43, 0
	v_mbcnt_lo_u32_b32 v0, -1, 0
	v_mbcnt_hi_u32_b32 v0, -1, v0
	v_and_b32_e32 v2, 31, v0
	v_lshrrev_b32_e32 v3, 5, v0
	s_lshl_b32 s21, s15, 5
	v_add_u32_e32 v2, s21, v2
	v_lshlrev_b32_e32 v2, 8, v2
	v_lshl_or_b32 v2, v3, 4, v2
	global_load_dwordx4 v[162:165], v2, s[40:41] offset:0
	global_load_dwordx4 v[166:169], v2, s[40:41] offset:32
	global_load_dwordx4 v[170:173], v2, s[40:41] offset:64
	global_load_dwordx4 v[174:177], v2, s[40:41] offset:96
	global_load_dwordx4 v[178:181], v2, s[40:41] offset:128
	global_load_dwordx4 v[182:185], v2, s[40:41] offset:160
	global_load_dwordx4 v[186:189], v2, s[40:41] offset:192
	global_load_dwordx4 v[190:193], v2, s[40:41] offset:224
	v_mov_b32_e32 v0, 0
	v_mov_b32_e32 v1, 0
	v_mov_b32_e32 v3, 0
	v_mov_b32_e32 v4, 0
	v_mov_b32_e32 v5, 0
	v_mov_b32_e32 v6, 0
	v_mov_b32_e32 v7, 0
	v_mov_b32_e32 v8, 0
	v_mov_b32_e32 v9, 0
	v_mov_b32_e32 v10, 0
	v_mov_b32_e32 v11, 0
	v_mov_b32_e32 v12, 0
	v_mov_b32_e32 v13, 0
	v_mov_b32_e32 v14, 0
	v_mov_b32_e32 v15, 0
	v_mov_b32_e32 v16, 0
	v_mov_b32_e32 v17, 0
	v_mov_b32_e32 v18, 0
	v_mov_b32_e32 v19, 0
	v_mov_b32_e32 v20, 0
	v_mov_b32_e32 v21, 0
	v_mov_b32_e32 v22, 0
	v_mov_b32_e32 v23, 0
	v_mov_b32_e32 v24, 0
	v_mov_b32_e32 v25, 0
	v_mov_b32_e32 v26, 0
	v_mov_b32_e32 v27, 0
	v_mov_b32_e32 v28, 0
	v_mov_b32_e32 v29, 0
	v_mov_b32_e32 v30, 0
	v_mov_b32_e32 v31, 0
	v_mov_b32_e32 v32, 0
	v_mov_b32_e32 v33, 0
	v_mov_b32_e32 v34, 0
	v_mov_b32_e32 v35, 0
	v_mov_b32_e32 v36, 0
	v_mov_b32_e32 v37, 0
	v_mov_b32_e32 v38, 0
	v_mov_b32_e32 v39, 0
	v_mov_b32_e32 v40, 0
	v_mov_b32_e32 v41, 0
	v_mov_b32_e32 v42, 0
	v_mov_b32_e32 v43, 0
	v_mov_b32_e32 v44, 0
	v_mov_b32_e32 v45, 0
	v_mov_b32_e32 v46, 0
	v_mov_b32_e32 v47, 0
	v_mov_b32_e32 v48, 0
	v_mov_b32_e32 v49, 0
	v_mov_b32_e32 v50, 0
	v_mov_b32_e32 v51, 0
	v_mov_b32_e32 v52, 0
	v_mov_b32_e32 v53, 0
	v_mov_b32_e32 v54, 0
	v_mov_b32_e32 v55, 0
	v_mov_b32_e32 v56, 0
	v_mov_b32_e32 v57, 0
	v_mov_b32_e32 v58, 0
	v_mov_b32_e32 v59, 0
	v_mov_b32_e32 v60, 0
	v_mov_b32_e32 v61, 0
	v_mov_b32_e32 v62, 0
	v_mov_b32_e32 v63, 0
	v_mov_b32_e32 v64, 0
	v_mov_b32_e32 v65, 0
	v_mov_b32_e32 v66, 0
	v_mov_b32_e32 v67, 0
	v_mov_b32_e32 v68, 0
	v_mov_b32_e32 v69, 0
	v_mov_b32_e32 v70, 0
	v_mov_b32_e32 v71, 0
	v_mov_b32_e32 v72, 0
	v_mov_b32_e32 v73, 0
	v_mov_b32_e32 v74, 0
	v_mov_b32_e32 v75, 0
	v_mov_b32_e32 v76, 0
	v_mov_b32_e32 v77, 0
	v_mov_b32_e32 v78, 0
	v_mov_b32_e32 v79, 0
	v_mov_b32_e32 v80, 0
	v_mov_b32_e32 v81, 0
	v_mov_b32_e32 v82, 0
	v_mov_b32_e32 v83, 0
	v_mov_b32_e32 v84, 0
	v_mov_b32_e32 v85, 0
	v_mov_b32_e32 v86, 0
	v_mov_b32_e32 v87, 0
	v_mov_b32_e32 v88, 0
	v_mov_b32_e32 v89, 0
	v_mov_b32_e32 v90, 0
	v_mov_b32_e32 v91, 0
	v_mov_b32_e32 v92, 0
	v_mov_b32_e32 v93, 0
	v_mov_b32_e32 v94, 0
	v_mov_b32_e32 v95, 0
	v_mov_b32_e32 v98, 0
	v_mov_b32_e32 v99, 0
	v_mov_b32_e32 v100, 0
	v_mov_b32_e32 v101, 0
	v_mov_b32_e32 v102, 0
	v_mov_b32_e32 v103, 0
	v_mov_b32_e32 v104, 0
	v_mov_b32_e32 v105, 0
	v_mov_b32_e32 v106, 0
	v_mov_b32_e32 v107, 0
	v_mov_b32_e32 v108, 0
	v_mov_b32_e32 v109, 0
	v_mov_b32_e32 v110, 0
	v_mov_b32_e32 v111, 0
	v_mov_b32_e32 v112, 0
	v_mov_b32_e32 v113, 0
	v_mov_b32_e32 v114, 0
	v_mov_b32_e32 v115, 0
	v_mov_b32_e32 v116, 0
	v_mov_b32_e32 v117, 0
	v_mov_b32_e32 v118, 0
	v_mov_b32_e32 v119, 0
	v_mov_b32_e32 v120, 0
	v_mov_b32_e32 v121, 0
	v_mov_b32_e32 v122, 0
	v_mov_b32_e32 v123, 0
	v_mov_b32_e32 v124, 0
	v_mov_b32_e32 v125, 0
	v_mov_b32_e32 v126, 0
	v_mov_b32_e32 v127, 0
	v_mov_b32_e32 v128, 0
	v_mov_b32_e32 v129, 0
	v_mov_b32_e32 v2, 0
	v_mov_b32_e32 v96, 0xf149f2ca
	v_mov_b32_e32 v202, 0
	s_add_i32 s5, s8, 1
	s_lshl_b32 s5, s5, 2
	s_lshl_b32 s14, s8, 2
	s_lshr_b32 s21, s15, 1
	s_add_i32 s14, s14, s21
	s_lshl_b32 s24, s8, 8
	s_lshl_b32 s21, s15, 5
	s_add_i32 s24, s24, s21
	s_mov_b32 s4, 0
	v_mbcnt_lo_u32_b32 v216, -1, 0
	v_mbcnt_hi_u32_b32 v216, -1, v216
	s_add_i32 s21, s20, 0x1e800
	v_lshl_add_u32 v216, v216, 2, s21
	ds_read_b32 v212, v216
	ds_read_b32 v213, v216 offset:256
	ds_read_b32 v214, v216 offset:512
	ds_read_b32 v215, v216 offset:768
	s_waitcnt lgkmcnt(0)
	s_mov_b32 s64, 0x0
	s_add_i32 s21, s64, s20
	s_mov_b32 m0, s21
	s_nop 0
	global_load_lds_dwordx4 v212, s[28:29]
	s_add_i32 m0, s21, 0x2000
	s_nop 0
	global_load_lds_dwordx4 v213, s[28:29]
	s_add_u32 s28, s28, 0x4000
	s_addc_u32 s29, s29, 0
	s_mov_b32 s65, 0x8000
	s_add_i32 s21, s65, s20
	s_mov_b32 m0, s21
	s_nop 0
	global_load_lds_dwordx4 v214, s[34:35]
	s_add_i32 m0, s21, 0x2000
	s_nop 0
	global_load_lds_dwordx4 v215, s[34:35]
	s_add_i32 m0, s21, 0x4000
	s_nop 0
	global_load_lds_dwordx4 v214, s[38:39]
	s_add_i32 m0, s21, 0x6000
	s_nop 0
	global_load_lds_dwordx4 v215, s[38:39]
	s_add_u32 s34, s34, 0x4000
	s_addc_u32 s35, s35, 0
	s_add_u32 s38, s38, 0x4000
	s_addc_u32 s39, s39, 0
.Lfa_tile:
	s_waitcnt vmcnt(0)
	s_barrier
	s_and_b32 s83, s4, 1
	s_lshl_b32 s84, s83, 15
	s_lshl_b32 s83, s83, 14
	s_add_i32 s84, s84, 0x8000
	v_add_u32_e32 v248, s83, v208
	s_movk_i32 s82, 0
	v_xad_u32 v244, v209, s82, v248
	s_movk_i32 s82, 32
	v_xad_u32 v245, v209, s82, v248
	s_movk_i32 s82, 64
	v_xad_u32 v246, v209, s82, v248
	s_movk_i32 s82, 96
	v_xad_u32 v247, v209, s82, v248
	ds_read_b128 v[228:231], v244 offset:0
	ds_read_b128 v[232:235], v244 offset:8192
	ds_read_b128 v[236:239], v245 offset:0
	ds_read_b128 v[240:243], v245 offset:8192
	s_add_i32 s78, s4, 1
	s_cmp_lt_u32 s78, s5
	s_cbranch_scc0 .Lfa_nodma
	v_mbcnt_lo_u32_b32 v216, -1, 0
	v_mbcnt_hi_u32_b32 v216, -1, v216
	s_add_i32 s21, s20, 0x1e800
	v_lshl_add_u32 v216, v216, 2, s21
	ds_read_b32 v212, v216
	ds_read_b32 v213, v216 offset:256
	ds_read_b32 v214, v216 offset:512
	ds_read_b32 v215, v216 offset:768
	s_waitcnt lgkmcnt(0)
	s_and_b32 s64, s78, 1
	s_lshl_b32 s65, s64, 15
	s_lshl_b32 s64, s64, 14
	s_add_i32 s65, s65, 0x8000
	s_add_i32 s21, s64, s20
	s_mov_b32 m0, s21
	s_nop 0
	global_load_lds_dwordx4 v212, s[28:29]
	s_add_i32 m0, s21, 0x2000
	s_nop 0
	global_load_lds_dwordx4 v213, s[28:29]
	s_add_u32 s28, s28, 0x4000
	s_addc_u32 s29, s29, 0
	s_add_i32 s21, s65, s20
	s_mov_b32 m0, s21
	s_nop 0
	global_load_lds_dwordx4 v214, s[34:35]
	s_add_i32 m0, s21, 0x2000
	s_nop 0
	global_load_lds_dwordx4 v215, s[34:35]
	s_add_i32 m0, s21, 0x4000
	s_nop 0
	global_load_lds_dwordx4 v214, s[38:39]
	s_add_i32 m0, s21, 0x6000
	s_nop 0
	global_load_lds_dwordx4 v215, s[38:39]
	s_add_u32 s34, s34, 0x4000
	s_addc_u32 s35, s35, 0
	s_add_u32 s38, s38, 0x4000
	s_addc_u32 s39, s39, 0
.Lfa_nodma:
	s_waitcnt lgkmcnt(2)
	v_mfma_f32_32x32x16_bf16 v[130:145], v[228:231], v[162:165], 0
	v_mfma_f32_32x32x16_bf16 v[146:161], v[232:235], v[162:165], 0
	ds_read_b128 v[228:231], v246 offset:0
	ds_read_b128 v[232:235], v246 offset:8192
	s_waitcnt lgkmcnt(2)
	v_mfma_f32_32x32x16_bf16 v[130:145], v[236:239], v[166:169], v[130:145]
	v_mfma_f32_32x32x16_bf16 v[146:161], v[240:243], v[166:169], v[146:161]
	ds_read_b128 v[236:239], v247 offset:0
	ds_read_b128 v[240:243], v247 offset:8192
	s_waitcnt lgkmcnt(2)
	v_mfma_f32_32x32x16_bf16 v[130:145], v[228:231], v[170:173], v[130:145]
	v_mfma_f32_32x32x16_bf16 v[146:161], v[232:235], v[170:173], v[146:161]
	ds_read_b128 v[228:231], v244 offset:128
	ds_read_b128 v[232:235], v244 offset:8320
	s_waitcnt lgkmcnt(2)
	v_mfma_f32_32x32x16_bf16 v[130:145], v[236:239], v[174:177], v[130:145]
	v_mfma_f32_32x32x16_bf16 v[146:161], v[240:243], v[174:177], v[146:161]
	ds_read_b128 v[236:239], v245 offset:128
	ds_read_b128 v[240:243], v245 offset:8320
	s_waitcnt lgkmcnt(2)
	v_mfma_f32_32x32x16_bf16 v[130:145], v[228:231], v[178:181], v[130:145]
	v_mfma_f32_32x32x16_bf16 v[146:161], v[232:235], v[178:181], v[146:161]
	ds_read_b128 v[228:231], v246 offset:128
	ds_read_b128 v[232:235], v246 offset:8320
	s_waitcnt lgkmcnt(2)
	v_mfma_f32_32x32x16_bf16 v[130:145], v[236:239], v[182:185], v[130:145]
	v_mfma_f32_32x32x16_bf16 v[146:161], v[240:243], v[182:185], v[146:161]
	ds_read_b128 v[236:239], v247 offset:128
	ds_read_b128 v[240:243], v247 offset:8320
	s_waitcnt lgkmcnt(2)
	v_mfma_f32_32x32x16_bf16 v[130:145], v[228:231], v[186:189], v[130:145]
	v_mfma_f32_32x32x16_bf16 v[146:161], v[232:235], v[186:189], v[146:161]
	s_waitcnt lgkmcnt(0)
	v_mfma_f32_32x32x16_bf16 v[130:145], v[236:239], v[190:193], v[130:145]
	v_mfma_f32_32x32x16_bf16 v[146:161], v[240:243], v[190:193], v[146:161]
	v_add_u32_e32 v253, s84, v210
	ds_read_b64_tr_b16 v[228:229], v253 offset:0
	ds_read_b64_tr_b16 v[230:231], v253 offset:2048
	ds_read_b64_tr_b16 v[232:233], v253 offset:4096
	ds_read_b64_tr_b16 v[234:235], v253 offset:6144
	ds_read_b64_tr_b16 v[236:237], v253 offset:8192
	ds_read_b64_tr_b16 v[238:239], v253 offset:10240
	ds_read_b64_tr_b16 v[240:241], v253 offset:12288
	ds_read_b64_tr_b16 v[242:243], v253 offset:14336
	ds_read_b64_tr_b16 v[244:245], v253 offset:512
	ds_read_b64_tr_b16 v[246:247], v253 offset:2560
	ds_read_b64_tr_b16 v[248:249], v253 offset:4608
	ds_read_b64_tr_b16 v[250:251], v253 offset:6656
	ds_read_b64_tr_b16 v[194:195], v253 offset:8704
	ds_read_b64_tr_b16 v[196:197], v253 offset:10752
	ds_read_b64_tr_b16 v[198:199], v253 offset:12800
	ds_read_b64_tr_b16 v[200:201], v253 offset:14848
	s_cmp_ge_u32 s4, s14
	s_cbranch_scc0 .Lfa_nomask
	v_mbcnt_lo_u32_b32 v206, -1, 0
	v_mbcnt_hi_u32_b32 v206, -1, v206
	v_and_b32_e32 v203, 31, v206
	v_lshrrev_b32_e32 v206, 5, v206
	v_lshlrev_b32_e32 v206, 2, v206
	v_sub_u32_e32 v203, v203, v206
	s_lshl_b32 s21, s4, 6
	s_sub_i32 s21, s24, s21
	v_add_u32_e32 v203, s21, v203
	v_mov_b32_e32 v204, 0xff800000
	v_cmp_gt_i32_e64 vcc, 0, v203
	v_cmp_gt_i32_e64 s[48:49], 32, v203
	v_cmp_gt_i32_e64 s[50:51], 1, v203
	v_cmp_gt_i32_e64 s[52:53], 33, v203
	v_cndmask_b32_e64 v130, v130, v204, vcc
	v_cndmask_b32_e64 v146, v146, v204, s[48:49]
	v_cndmask_b32_e64 v131, v131, v204, s[50:51]
	v_cndmask_b32_e64 v147, v147, v204, s[52:53]
	v_cmp_gt_i32_e64 vcc, 2, v203
	v_cmp_gt_i32_e64 s[48:49], 34, v203
	v_cmp_gt_i32_e64 s[50:51], 3, v203
	v_cmp_gt_i32_e64 s[52:53], 35, v203
	v_cndmask_b32_e64 v132, v132, v204, vcc
	v_cndmask_b32_e64 v148, v148, v204, s[48:49]
	v_cndmask_b32_e64 v133, v133, v204, s[50:51]
	v_cndmask_b32_e64 v149, v149, v204, s[52:53]
	v_cmp_gt_i32_e64 vcc, 8, v203
	v_cmp_gt_i32_e64 s[48:49], 40, v203
	v_cmp_gt_i32_e64 s[50:51], 9, v203
	v_cmp_gt_i32_e64 s[52:53], 41, v203
	v_cndmask_b32_e64 v134, v134, v204, vcc
	v_cndmask_b32_e64 v150, v150, v204, s[48:49]
	v_cndmask_b32_e64 v135, v135, v204, s[50:51]
	v_cndmask_b32_e64 v151, v151, v204, s[52:53]
	v_cmp_gt_i32_e64 vcc, 10, v203
	v_cmp_gt_i32_e64 s[48:49], 42, v203
	v_cmp_gt_i32_e64 s[50:51], 11, v203
	v_cmp_gt_i32_e64 s[52:53], 43, v203
	v_cndmask_b32_e64 v136, v136, v204, vcc
	v_cndmask_b32_e64 v152, v152, v204, s[48:49]
	v_cndmask_b32_e64 v137, v137, v204, s[50:51]
	v_cndmask_b32_e64 v153, v153, v204, s[52:53]
	v_cmp_gt_i32_e64 vcc, 16, v203
	v_cmp_gt_i32_e64 s[48:49], 48, v203
	v_cmp_gt_i32_e64 s[50:51], 17, v203
	v_cmp_gt_i32_e64 s[52:53], 49, v203
	v_cndmask_b32_e64 v138, v138, v204, vcc
	v_cndmask_b32_e64 v154, v154, v204, s[48:49]
	v_cndmask_b32_e64 v139, v139, v204, s[50:51]
	v_cndmask_b32_e64 v155, v155, v204, s[52:53]
	v_cmp_gt_i32_e64 vcc, 18, v203
	v_cmp_gt_i32_e64 s[48:49], 50, v203
	v_cmp_gt_i32_e64 s[50:51], 19, v203
	v_cmp_gt_i32_e64 s[52:53], 51, v203
	v_cndmask_b32_e64 v140, v140, v204, vcc
	v_cndmask_b32_e64 v156, v156, v204, s[48:49]
	v_cndmask_b32_e64 v141, v141, v204, s[50:51]
	v_cndmask_b32_e64 v157, v157, v204, s[52:53]
	v_cmp_gt_i32_e64 vcc, 24, v203
	v_cmp_gt_i32_e64 s[48:49], 56, v203
	v_cmp_gt_i32_e64 s[50:51], 25, v203
	v_cmp_gt_i32_e64 s[52:53], 57, v203
	v_cndmask_b32_e64 v142, v142, v204, vcc
	v_cndmask_b32_e64 v158, v158, v204, s[48:49]
	v_cndmask_b32_e64 v143, v143, v204, s[50:51]
	v_cndmask_b32_e64 v159, v159, v204, s[52:53]
	v_cmp_gt_i32_e64 vcc, 26, v203
	v_cmp_gt_i32_e64 s[48:49], 58, v203
	v_cmp_gt_i32_e64 s[50:51], 27, v203
	v_cmp_gt_i32_e64 s[52:53], 59, v203
	v_cndmask_b32_e64 v144, v144, v204, vcc
	v_cndmask_b32_e64 v160, v160, v204, s[48:49]
	v_cndmask_b32_e64 v145, v145, v204, s[50:51]
	v_cndmask_b32_e64 v161, v161, v204, s[52:53]
.Lfa_nomask:
	v_max3_f32 v203, v130, v131, v132
	v_max3_f32 v203, v203, v133, v134
	v_max3_f32 v203, v203, v135, v136
	v_max3_f32 v203, v203, v137, v138
	v_max3_f32 v203, v203, v139, v140
	v_max3_f32 v203, v203, v141, v142
	v_max3_f32 v203, v203, v143, v144
	v_max3_f32 v203, v203, v145, v146
	v_max3_f32 v203, v203, v147, v148
	v_max3_f32 v203, v203, v149, v150
	v_max3_f32 v203, v203, v151, v152
	v_max3_f32 v203, v203, v153, v154
	v_max3_f32 v203, v203, v155, v156
	v_max3_f32 v203, v203, v157, v158
	v_max3_f32 v203, v203, v159, v160
	v_max_f32_e32 v203, v203, v161
	v_mov_b32_e32 v204, v203
	s_nop 1
	v_permlane32_swap_b32_e32 v203, v204
	v_max_f32_e32 v203, v203, v204
	v_sub_f32_e32 v204, v203, v96
	v_mov_b32_e32 v207, 0x42b504f3
	v_cmp_gt_f32_e32 vcc, v204, v207
	s_cmp_lg_u64 vcc, 0
	s_cselect_b64 s[92:93], -1, 0
	v_max_f32_e32 v204, v96, v203
	s_nop 0
	v_cndmask_b32_e64 v207, v96, v204, s[92:93]
	v_sub_f32_e32 v206, v96, v207
	v_mul_f32_e32 v206, 0x3e0293ee, v206
	v_exp_f32_e32 v206, v206
	v_mov_b32_e32 v96, v207
	v_mul_f32_e32 v207, 0xbe0293ee, v207
	v_mov_b32_e32 v204, 0x3e0293ee
	v_mul_f32_e32 v202, v202, v206
	v_fma_f32 v130, v130, v204, v207
	v_fma_f32 v131, v131, v204, v207
	v_fma_f32 v132, v132, v204, v207
	v_fma_f32 v133, v133, v204, v207
	v_fma_f32 v134, v134, v204, v207
	v_fma_f32 v135, v135, v204, v207
	v_fma_f32 v136, v136, v204, v207
	v_fma_f32 v137, v137, v204, v207
	v_fma_f32 v138, v138, v204, v207
	v_fma_f32 v139, v139, v204, v207
	v_fma_f32 v140, v140, v204, v207
	v_fma_f32 v141, v141, v204, v207
	v_fma_f32 v142, v142, v204, v207
	v_fma_f32 v143, v143, v204, v207
	v_fma_f32 v144, v144, v204, v207
	v_fma_f32 v145, v145, v204, v207
	v_fma_f32 v146, v146, v204, v207
	v_fma_f32 v147, v147, v204, v207
	v_fma_f32 v148, v148, v204, v207
	v_fma_f32 v149, v149, v204, v207
	v_fma_f32 v150, v150, v204, v207
	v_fma_f32 v151, v151, v204, v207
	v_fma_f32 v152, v152, v204, v207
	v_fma_f32 v153, v153, v204, v207
	v_fma_f32 v154, v154, v204, v207
	v_fma_f32 v155, v155, v204, v207
	v_fma_f32 v156, v156, v204, v207
	v_fma_f32 v157, v157, v204, v207
	v_fma_f32 v158, v158, v204, v207
	v_fma_f32 v159, v159, v204, v207
	v_fma_f32 v160, v160, v204, v207
	v_fma_f32 v161, v161, v204, v207
	v_exp_f32_e32 v130, v130
	v_exp_f32_e32 v131, v131
	v_exp_f32_e32 v132, v132
	v_exp_f32_e32 v133, v133
	v_exp_f32_e32 v134, v134
	v_exp_f32_e32 v135, v135
	v_exp_f32_e32 v136, v136
	v_exp_f32_e32 v137, v137
	v_exp_f32_e32 v138, v138
	v_exp_f32_e32 v139, v139
	v_exp_f32_e32 v140, v140
	v_exp_f32_e32 v141, v141
	v_exp_f32_e32 v142, v142
	v_exp_f32_e32 v143, v143
	v_exp_f32_e32 v144, v144
	v_exp_f32_e32 v145, v145
	v_exp_f32_e32 v146, v146
	v_exp_f32_e32 v147, v147
	v_exp_f32_e32 v148, v148
	v_exp_f32_e32 v149, v149
	v_exp_f32_e32 v150, v150
	v_exp_f32_e32 v151, v151
	v_exp_f32_e32 v152, v152
	v_exp_f32_e32 v153, v153
	v_exp_f32_e32 v154, v154
	v_exp_f32_e32 v155, v155
	v_exp_f32_e32 v156, v156
	v_exp_f32_e32 v157, v157
	v_exp_f32_e32 v158, v158
	v_exp_f32_e32 v159, v159
	v_exp_f32_e32 v160, v160
	v_exp_f32_e32 v161, v161
	s_nop 0
	v_add_f32_e32 v252, v130, v131
	v_add_f32_e32 v252, v252, v132
	v_add_f32_e32 v252, v252, v133
	v_add_f32_e32 v252, v252, v134
	v_add_f32_e32 v252, v252, v135
	v_add_f32_e32 v252, v252, v136
	v_add_f32_e32 v252, v252, v137
	v_add_f32_e32 v252, v252, v138
	v_add_f32_e32 v252, v252, v139
	v_add_f32_e32 v252, v252, v140
	v_add_f32_e32 v252, v252, v141
	v_add_f32_e32 v252, v252, v142
	v_add_f32_e32 v252, v252, v143
	v_add_f32_e32 v252, v252, v144
	v_add_f32_e32 v252, v252, v145
	v_add_f32_e32 v252, v252, v146
	v_add_f32_e32 v252, v252, v147
	v_add_f32_e32 v252, v252, v148
	v_add_f32_e32 v252, v252, v149
	v_add_f32_e32 v252, v252, v150
	v_add_f32_e32 v252, v252, v151
	v_add_f32_e32 v252, v252, v152
	v_add_f32_e32 v252, v252, v153
	v_add_f32_e32 v252, v252, v154
	v_add_f32_e32 v252, v252, v155
	v_add_f32_e32 v252, v252, v156
	v_add_f32_e32 v252, v252, v157
	v_add_f32_e32 v252, v252, v158
	v_add_f32_e32 v252, v252, v159
	v_add_f32_e32 v252, v252, v160
	v_add_f32_e32 v252, v252, v161
	v_mov_b32_e32 v204, v252
	s_nop 1
	v_permlane32_swap_b32_e32 v252, v204
	v_add_f32_e32 v252, v252, v204
	v_add_f32_e32 v202, v202, v252
	v_cvt_pk_bf16_f32 v212, v130, v131
	v_cvt_pk_bf16_f32 v213, v132, v133
	v_cvt_pk_bf16_f32 v214, v134, v135
	v_cvt_pk_bf16_f32 v215, v136, v137
	v_cvt_pk_bf16_f32 v216, v138, v139
	v_cvt_pk_bf16_f32 v217, v140, v141
	v_cvt_pk_bf16_f32 v218, v142, v143
	v_cvt_pk_bf16_f32 v219, v144, v145
	v_cvt_pk_bf16_f32 v220, v146, v147
	v_cvt_pk_bf16_f32 v221, v148, v149
	v_cvt_pk_bf16_f32 v222, v150, v151
	v_cvt_pk_bf16_f32 v223, v152, v153
	v_cvt_pk_bf16_f32 v224, v154, v155
	v_cvt_pk_bf16_f32 v225, v156, v157
	v_cvt_pk_bf16_f32 v226, v158, v159
	v_cvt_pk_bf16_f32 v227, v160, v161
	s_nop 1
	v_permlane32_swap_b32_e32 v212, v214
	v_permlane32_swap_b32_e32 v213, v215
	v_permlane32_swap_b32_e32 v216, v218
	v_permlane32_swap_b32_e32 v217, v219
	v_permlane32_swap_b32_e32 v220, v222
	v_permlane32_swap_b32_e32 v221, v223
	v_permlane32_swap_b32_e32 v224, v226
	v_permlane32_swap_b32_e32 v225, v227
	s_and_b64 vcc, exec, s[92:93]
	s_cbranch_vccz .Lfa_noresc_t
	v_mbcnt_lo_u32_b32 v204, -1, 0
	v_mbcnt_hi_u32_b32 v204, -1, v204
	s_lshl_b32 s21, s15, 8
	s_add_i32 s21, s21, 0x18000
	v_and_b32_e32 v207, 31, v204
	v_lshl_add_u32 v207, v207, 2, s21
	v_lshrrev_b32_e32 v204, 5, v204
	v_lshl_add_u32 v204, v204, 4, s21
	ds_write_b32 v207, v206
	s_waitcnt lgkmcnt(0)
	ds_read_b128 v[236:239], v204 offset:0
	ds_read_b128 v[240:243], v204 offset:32
	ds_read_b128 v[244:247], v204 offset:64
	ds_read_b128 v[248:251], v204 offset:96
	s_waitcnt lgkmcnt(0)
	v_pk_mul_f32 v[0:1], v[0:1], v[236:237]
	v_pk_mul_f32 v[2:3], v[2:3], v[238:239]
	v_pk_mul_f32 v[4:5], v[4:5], v[240:241]
	v_pk_mul_f32 v[6:7], v[6:7], v[242:243]
	v_pk_mul_f32 v[8:9], v[8:9], v[244:245]
	v_pk_mul_f32 v[10:11], v[10:11], v[246:247]
	v_pk_mul_f32 v[12:13], v[12:13], v[248:249]
	v_pk_mul_f32 v[14:15], v[14:15], v[250:251]
	v_pk_mul_f32 v[16:17], v[16:17], v[236:237]
	v_pk_mul_f32 v[18:19], v[18:19], v[238:239]
	v_pk_mul_f32 v[20:21], v[20:21], v[240:241]
	v_pk_mul_f32 v[22:23], v[22:23], v[242:243]
	v_pk_mul_f32 v[24:25], v[24:25], v[244:245]
	v_pk_mul_f32 v[26:27], v[26:27], v[246:247]
	v_pk_mul_f32 v[28:29], v[28:29], v[248:249]
	v_pk_mul_f32 v[30:31], v[30:31], v[250:251]
	v_pk_mul_f32 v[32:33], v[32:33], v[236:237]
	v_pk_mul_f32 v[34:35], v[34:35], v[238:239]
	v_pk_mul_f32 v[36:37], v[36:37], v[240:241]
	v_pk_mul_f32 v[38:39], v[38:39], v[242:243]
	v_pk_mul_f32 v[40:41], v[40:41], v[244:245]
	v_pk_mul_f32 v[42:43], v[42:43], v[246:247]
	v_pk_mul_f32 v[44:45], v[44:45], v[248:249]
	v_pk_mul_f32 v[46:47], v[46:47], v[250:251]
	v_pk_mul_f32 v[48:49], v[48:49], v[236:237]
	v_pk_mul_f32 v[50:51], v[50:51], v[238:239]
	v_pk_mul_f32 v[52:53], v[52:53], v[240:241]
	v_pk_mul_f32 v[54:55], v[54:55], v[242:243]
	v_pk_mul_f32 v[56:57], v[56:57], v[244:245]
	v_pk_mul_f32 v[58:59], v[58:59], v[246:247]
	v_pk_mul_f32 v[60:61], v[60:61], v[248:249]
	v_pk_mul_f32 v[62:63], v[62:63], v[250:251]
	v_pk_mul_f32 v[64:65], v[64:65], v[236:237]
	v_pk_mul_f32 v[66:67], v[66:67], v[238:239]
	v_pk_mul_f32 v[68:69], v[68:69], v[240:241]
	v_pk_mul_f32 v[70:71], v[70:71], v[242:243]
	v_pk_mul_f32 v[72:73], v[72:73], v[244:245]
	v_pk_mul_f32 v[74:75], v[74:75], v[246:247]
	v_pk_mul_f32 v[76:77], v[76:77], v[248:249]
	v_pk_mul_f32 v[78:79], v[78:79], v[250:251]
	v_pk_mul_f32 v[80:81], v[80:81], v[236:237]
	v_pk_mul_f32 v[82:83], v[82:83], v[238:239]
	v_pk_mul_f32 v[84:85], v[84:85], v[240:241]
	v_pk_mul_f32 v[86:87], v[86:87], v[242:243]
	v_pk_mul_f32 v[88:89], v[88:89], v[244:245]
	v_pk_mul_f32 v[90:91], v[90:91], v[246:247]
	v_pk_mul_f32 v[92:93], v[92:93], v[248:249]
	v_pk_mul_f32 v[94:95], v[94:95], v[250:251]
	v_pk_mul_f32 v[98:99], v[98:99], v[236:237]
	v_pk_mul_f32 v[100:101], v[100:101], v[238:239]
	v_pk_mul_f32 v[102:103], v[102:103], v[240:241]
	v_pk_mul_f32 v[104:105], v[104:105], v[242:243]
	v_pk_mul_f32 v[106:107], v[106:107], v[244:245]
	v_pk_mul_f32 v[108:109], v[108:109], v[246:247]
	v_pk_mul_f32 v[110:111], v[110:111], v[248:249]
	v_pk_mul_f32 v[112:113], v[112:113], v[250:251]
	v_pk_mul_f32 v[114:115], v[114:115], v[236:237]
	v_pk_mul_f32 v[116:117], v[116:117], v[238:239]
	v_pk_mul_f32 v[118:119], v[118:119], v[240:241]
	v_pk_mul_f32 v[120:121], v[120:121], v[242:243]
	v_pk_mul_f32 v[122:123], v[122:123], v[244:245]
	v_pk_mul_f32 v[124:125], v[124:125], v[246:247]
	v_pk_mul_f32 v[126:127], v[126:127], v[248:249]
	v_pk_mul_f32 v[128:129], v[128:129], v[250:251]
	ds_read_b64_tr_b16 v[228:229], v253 offset:0
	ds_read_b64_tr_b16 v[230:231], v253 offset:2048
	ds_read_b64_tr_b16 v[232:233], v253 offset:4096
	ds_read_b64_tr_b16 v[234:235], v253 offset:6144
	ds_read_b64_tr_b16 v[236:237], v253 offset:8192
	ds_read_b64_tr_b16 v[238:239], v253 offset:10240
	ds_read_b64_tr_b16 v[240:241], v253 offset:12288
	ds_read_b64_tr_b16 v[242:243], v253 offset:14336
	ds_read_b64_tr_b16 v[244:245], v253 offset:512
	ds_read_b64_tr_b16 v[246:247], v253 offset:2560
	ds_read_b64_tr_b16 v[248:249], v253 offset:4608
	ds_read_b64_tr_b16 v[250:251], v253 offset:6656
	ds_read_b64_tr_b16 v[194:195], v253 offset:8704
	ds_read_b64_tr_b16 v[196:197], v253 offset:10752
	ds_read_b64_tr_b16 v[198:199], v253 offset:12800
	ds_read_b64_tr_b16 v[200:201], v253 offset:14848
.Lfa_noresc_t:
	s_waitcnt lgkmcnt(8)
	v_mfma_f32_32x32x16_bf16 v[0:15], v[212:215], v[228:231], v[0:15]
	v_mfma_f32_32x32x16_bf16 v[0:15], v[216:219], v[232:235], v[0:15]
	v_mfma_f32_32x32x16_bf16 v[0:15], v[220:223], v[236:239], v[0:15]
	v_mfma_f32_32x32x16_bf16 v[0:15], v[224:227], v[240:243], v[0:15]
	ds_read_b64_tr_b16 v[228:229], v253 offset:1024
	ds_read_b64_tr_b16 v[230:231], v253 offset:3072
	ds_read_b64_tr_b16 v[232:233], v253 offset:5120
	ds_read_b64_tr_b16 v[234:235], v253 offset:7168
	ds_read_b64_tr_b16 v[236:237], v253 offset:9216
	ds_read_b64_tr_b16 v[238:239], v253 offset:11264
	ds_read_b64_tr_b16 v[240:241], v253 offset:13312
	ds_read_b64_tr_b16 v[242:243], v253 offset:15360
	s_waitcnt lgkmcnt(8)
	v_mfma_f32_32x32x16_bf16 v[16:31], v[212:215], v[244:247], v[16:31]
	v_mfma_f32_32x32x16_bf16 v[16:31], v[216:219], v[248:251], v[16:31]
	v_mfma_f32_32x32x16_bf16 v[16:31], v[220:223], v[194:197], v[16:31]
	v_mfma_f32_32x32x16_bf16 v[16:31], v[224:227], v[198:201], v[16:31]
	ds_read_b64_tr_b16 v[244:245], v253 offset:1536
	ds_read_b64_tr_b16 v[246:247], v253 offset:3584
	ds_read_b64_tr_b16 v[248:249], v253 offset:5632
	ds_read_b64_tr_b16 v[250:251], v253 offset:7680
	ds_read_b64_tr_b16 v[194:195], v253 offset:9728
	ds_read_b64_tr_b16 v[196:197], v253 offset:11776
	ds_read_b64_tr_b16 v[198:199], v253 offset:13824
	ds_read_b64_tr_b16 v[200:201], v253 offset:15872
	s_waitcnt lgkmcnt(8)
	v_mfma_f32_32x32x16_bf16 v[32:47], v[212:215], v[228:231], v[32:47]
	v_mfma_f32_32x32x16_bf16 v[32:47], v[216:219], v[232:235], v[32:47]
	v_mfma_f32_32x32x16_bf16 v[32:47], v[220:223], v[236:239], v[32:47]
	v_mfma_f32_32x32x16_bf16 v[32:47], v[224:227], v[240:243], v[32:47]
	ds_read_b64_tr_b16 v[228:229], v253 offset:16384
	ds_read_b64_tr_b16 v[230:231], v253 offset:18432
	ds_read_b64_tr_b16 v[232:233], v253 offset:20480
	ds_read_b64_tr_b16 v[234:235], v253 offset:22528
	ds_read_b64_tr_b16 v[236:237], v253 offset:24576
	ds_read_b64_tr_b16 v[238:239], v253 offset:26624
	ds_read_b64_tr_b16 v[240:241], v253 offset:28672
	ds_read_b64_tr_b16 v[242:243], v253 offset:30720
	s_waitcnt lgkmcnt(8)
	v_mfma_f32_32x32x16_bf16 v[48:63], v[212:215], v[244:247], v[48:63]
	v_mfma_f32_32x32x16_bf16 v[48:63], v[216:219], v[248:251], v[48:63]
	v_mfma_f32_32x32x16_bf16 v[48:63], v[220:223], v[194:197], v[48:63]
	v_mfma_f32_32x32x16_bf16 v[48:63], v[224:227], v[198:201], v[48:63]
	ds_read_b64_tr_b16 v[244:245], v253 offset:16896
	ds_read_b64_tr_b16 v[246:247], v253 offset:18944
	ds_read_b64_tr_b16 v[248:249], v253 offset:20992
	ds_read_b64_tr_b16 v[250:251], v253 offset:23040
	ds_read_b64_tr_b16 v[194:195], v253 offset:25088
	ds_read_b64_tr_b16 v[196:197], v253 offset:27136
	ds_read_b64_tr_b16 v[198:199], v253 offset:29184
	ds_read_b64_tr_b16 v[200:201], v253 offset:31232
	s_waitcnt lgkmcnt(8)
	v_mfma_f32_32x32x16_bf16 v[64:79], v[212:215], v[228:231], v[64:79]
	v_mfma_f32_32x32x16_bf16 v[64:79], v[216:219], v[232:235], v[64:79]
	v_mfma_f32_32x32x16_bf16 v[64:79], v[220:223], v[236:239], v[64:79]
	v_mfma_f32_32x32x16_bf16 v[64:79], v[224:227], v[240:243], v[64:79]
	ds_read_b64_tr_b16 v[228:229], v253 offset:17408
	ds_read_b64_tr_b16 v[230:231], v253 offset:19456
	ds_read_b64_tr_b16 v[232:233], v253 offset:21504
	ds_read_b64_tr_b16 v[234:235], v253 offset:23552
	ds_read_b64_tr_b16 v[236:237], v253 offset:25600
	ds_read_b64_tr_b16 v[238:239], v253 offset:27648
	ds_read_b64_tr_b16 v[240:241], v253 offset:29696
	ds_read_b64_tr_b16 v[242:243], v253 offset:31744
	s_waitcnt lgkmcnt(8)
	v_mfma_f32_32x32x16_bf16 v[80:95], v[212:215], v[244:247], v[80:95]
	v_mfma_f32_32x32x16_bf16 v[80:95], v[216:219], v[248:251], v[80:95]
	v_mfma_f32_32x32x16_bf16 v[80:95], v[220:223], v[194:197], v[80:95]
	v_mfma_f32_32x32x16_bf16 v[80:95], v[224:227], v[198:201], v[80:95]
	ds_read_b64_tr_b16 v[244:245], v253 offset:17920
	ds_read_b64_tr_b16 v[246:247], v253 offset:19968
	ds_read_b64_tr_b16 v[248:249], v253 offset:22016
	ds_read_b64_tr_b16 v[250:251], v253 offset:24064
	ds_read_b64_tr_b16 v[194:195], v253 offset:26112
	ds_read_b64_tr_b16 v[196:197], v253 offset:28160
	ds_read_b64_tr_b16 v[198:199], v253 offset:30208
	ds_read_b64_tr_b16 v[200:201], v253 offset:32256
	s_waitcnt lgkmcnt(8)
	v_mfma_f32_32x32x16_bf16 v[98:113], v[212:215], v[228:231], v[98:113]
	v_mfma_f32_32x32x16_bf16 v[98:113], v[216:219], v[232:235], v[98:113]
	v_mfma_f32_32x32x16_bf16 v[98:113], v[220:223], v[236:239], v[98:113]
	v_mfma_f32_32x32x16_bf16 v[98:113], v[224:227], v[240:243], v[98:113]
	s_waitcnt lgkmcnt(0)
	v_mfma_f32_32x32x16_bf16 v[114:129], v[212:215], v[244:247], v[114:129]
	v_mfma_f32_32x32x16_bf16 v[114:129], v[216:219], v[248:251], v[114:129]
	v_mfma_f32_32x32x16_bf16 v[114:129], v[220:223], v[194:197], v[114:129]
	v_mfma_f32_32x32x16_bf16 v[114:129], v[224:227], v[198:201], v[114:129]
	s_add_i32 s4, s4, 1
	s_cmp_lt_u32 s4, s5
	s_cbranch_scc1 .Lfa_tile
	s_nop 7
	s_nop 7
	v_mbcnt_lo_u32_b32 v229, -1, 0
	v_mbcnt_hi_u32_b32 v229, -1, v229
	s_lshl_b32 s21, s15, 8
	s_add_i32 s21, s21, 0x18000
	v_and_b32_e32 v231, 31, v229
	v_lshl_add_u32 v230, v231, 2, s21
	v_lshrrev_b32_e32 v229, 5, v229
	v_lshl_add_u32 v232, v229, 4, s21
	ds_write_b32 v230, v202 offset:128
	s_waitcnt lgkmcnt(0)
	ds_read_b128 v[236:239], v232 offset:128
	ds_read_b128 v[240:243], v232 offset:160
	ds_read_b128 v[244:247], v232 offset:192
	ds_read_b128 v[248:251], v232 offset:224
	s_lshl_b32 s21, s15, 13
	v_lshlrev_b32_e32 v233, 10, v229
	v_lshl_add_u32 v233, v231, 1, v233
	v_add_u32_e32 v233, s21, v233
	v_add_u32_e32 v234, 0x1000, v233
	s_waitcnt lgkmcnt(0)
	v_rcp_f32_e32 v236, v236
	v_rcp_f32_e32 v237, v237
	v_rcp_f32_e32 v238, v238
	v_rcp_f32_e32 v239, v239
	v_rcp_f32_e32 v240, v240
	v_rcp_f32_e32 v241, v241
	v_rcp_f32_e32 v242, v242
	v_rcp_f32_e32 v243, v243
	v_rcp_f32_e32 v244, v244
	v_rcp_f32_e32 v245, v245
	v_rcp_f32_e32 v246, v246
	v_rcp_f32_e32 v247, v247
	v_rcp_f32_e32 v248, v248
	v_rcp_f32_e32 v249, v249
	v_rcp_f32_e32 v250, v250
	v_rcp_f32_e32 v251, v251
	s_nop 0
	v_mul_f32_dpp v228, v0, v236 quad_perm:[1,0,3,2] row_mask:0xf bank_mask:0xf
	v_mul_f32_e32 v0, v0, v236
	v_cvt_pk_bf16_f32 v0, v0, v228
	v_mul_f32_dpp v228, v1, v237 quad_perm:[1,0,3,2] row_mask:0xf bank_mask:0xf
	v_mul_f32_e32 v1, v1, v237
	v_cvt_pk_bf16_f32 v1, v1, v228
	v_mul_f32_dpp v228, v2, v238 quad_perm:[1,0,3,2] row_mask:0xf bank_mask:0xf
	v_mul_f32_e32 v2, v2, v238
	v_cvt_pk_bf16_f32 v2, v2, v228
	v_mul_f32_dpp v228, v3, v239 quad_perm:[1,0,3,2] row_mask:0xf bank_mask:0xf
	v_mul_f32_e32 v3, v3, v239
	v_cvt_pk_bf16_f32 v3, v3, v228
	v_mul_f32_dpp v228, v4, v240 quad_perm:[1,0,3,2] row_mask:0xf bank_mask:0xf
	v_mul_f32_e32 v4, v4, v240
	v_cvt_pk_bf16_f32 v4, v4, v228
	v_mul_f32_dpp v228, v5, v241 quad_perm:[1,0,3,2] row_mask:0xf bank_mask:0xf
	v_mul_f32_e32 v5, v5, v241
	v_cvt_pk_bf16_f32 v5, v5, v228
	v_mul_f32_dpp v228, v6, v242 quad_perm:[1,0,3,2] row_mask:0xf bank_mask:0xf
	v_mul_f32_e32 v6, v6, v242
	v_cvt_pk_bf16_f32 v6, v6, v228
	v_mul_f32_dpp v228, v7, v243 quad_perm:[1,0,3,2] row_mask:0xf bank_mask:0xf
	v_mul_f32_e32 v7, v7, v243
	v_cvt_pk_bf16_f32 v7, v7, v228
	v_mul_f32_dpp v228, v8, v244 quad_perm:[1,0,3,2] row_mask:0xf bank_mask:0xf
	v_mul_f32_e32 v8, v8, v244
	v_cvt_pk_bf16_f32 v8, v8, v228
	v_mul_f32_dpp v228, v9, v245 quad_perm:[1,0,3,2] row_mask:0xf bank_mask:0xf
	v_mul_f32_e32 v9, v9, v245
	v_cvt_pk_bf16_f32 v9, v9, v228
	v_mul_f32_dpp v228, v10, v246 quad_perm:[1,0,3,2] row_mask:0xf bank_mask:0xf
	v_mul_f32_e32 v10, v10, v246
	v_cvt_pk_bf16_f32 v10, v10, v228
	v_mul_f32_dpp v228, v11, v247 quad_perm:[1,0,3,2] row_mask:0xf bank_mask:0xf
	v_mul_f32_e32 v11, v11, v247
	v_cvt_pk_bf16_f32 v11, v11, v228
	v_mul_f32_dpp v228, v12, v248 quad_perm:[1,0,3,2] row_mask:0xf bank_mask:0xf
	v_mul_f32_e32 v12, v12, v248
	v_cvt_pk_bf16_f32 v12, v12, v228
	v_mul_f32_dpp v228, v13, v249 quad_perm:[1,0,3,2] row_mask:0xf bank_mask:0xf
	v_mul_f32_e32 v13, v13, v249
	v_cvt_pk_bf16_f32 v13, v13, v228
	v_mul_f32_dpp v228, v14, v250 quad_perm:[1,0,3,2] row_mask:0xf bank_mask:0xf
	v_mul_f32_e32 v14, v14, v250
	v_cvt_pk_bf16_f32 v14, v14, v228
	v_mul_f32_dpp v228, v15, v251 quad_perm:[1,0,3,2] row_mask:0xf bank_mask:0xf
	v_mul_f32_e32 v15, v15, v251
	v_cvt_pk_bf16_f32 v15, v15, v228
	v_mul_f32_dpp v228, v16, v236 quad_perm:[1,0,3,2] row_mask:0xf bank_mask:0xf
	v_mul_f32_e32 v16, v16, v236
	v_cvt_pk_bf16_f32 v16, v16, v228
	v_mul_f32_dpp v228, v17, v237 quad_perm:[1,0,3,2] row_mask:0xf bank_mask:0xf
	v_mul_f32_e32 v17, v17, v237
	v_cvt_pk_bf16_f32 v17, v17, v228
	v_mul_f32_dpp v228, v18, v238 quad_perm:[1,0,3,2] row_mask:0xf bank_mask:0xf
	v_mul_f32_e32 v18, v18, v238
	v_cvt_pk_bf16_f32 v18, v18, v228
	v_mul_f32_dpp v228, v19, v239 quad_perm:[1,0,3,2] row_mask:0xf bank_mask:0xf
	v_mul_f32_e32 v19, v19, v239
	v_cvt_pk_bf16_f32 v19, v19, v228
	v_mul_f32_dpp v228, v20, v240 quad_perm:[1,0,3,2] row_mask:0xf bank_mask:0xf
	v_mul_f32_e32 v20, v20, v240
	v_cvt_pk_bf16_f32 v20, v20, v228
	v_mul_f32_dpp v228, v21, v241 quad_perm:[1,0,3,2] row_mask:0xf bank_mask:0xf
	v_mul_f32_e32 v21, v21, v241
	v_cvt_pk_bf16_f32 v21, v21, v228
	v_mul_f32_dpp v228, v22, v242 quad_perm:[1,0,3,2] row_mask:0xf bank_mask:0xf
	v_mul_f32_e32 v22, v22, v242
	v_cvt_pk_bf16_f32 v22, v22, v228
	v_mul_f32_dpp v228, v23, v243 quad_perm:[1,0,3,2] row_mask:0xf bank_mask:0xf
	v_mul_f32_e32 v23, v23, v243
	v_cvt_pk_bf16_f32 v23, v23, v228
	v_mul_f32_dpp v228, v24, v244 quad_perm:[1,0,3,2] row_mask:0xf bank_mask:0xf
	v_mul_f32_e32 v24, v24, v244
	v_cvt_pk_bf16_f32 v24, v24, v228
	v_mul_f32_dpp v228, v25, v245 quad_perm:[1,0,3,2] row_mask:0xf bank_mask:0xf
	v_mul_f32_e32 v25, v25, v245
	v_cvt_pk_bf16_f32 v25, v25, v228
	v_mul_f32_dpp v228, v26, v246 quad_perm:[1,0,3,2] row_mask:0xf bank_mask:0xf
	v_mul_f32_e32 v26, v26, v246
	v_cvt_pk_bf16_f32 v26, v26, v228
	v_mul_f32_dpp v228, v27, v247 quad_perm:[1,0,3,2] row_mask:0xf bank_mask:0xf
	v_mul_f32_e32 v27, v27, v247
	v_cvt_pk_bf16_f32 v27, v27, v228
	v_mul_f32_dpp v228, v28, v248 quad_perm:[1,0,3,2] row_mask:0xf bank_mask:0xf
	v_mul_f32_e32 v28, v28, v248
	v_cvt_pk_bf16_f32 v28, v28, v228
	v_mul_f32_dpp v228, v29, v249 quad_perm:[1,0,3,2] row_mask:0xf bank_mask:0xf
	v_mul_f32_e32 v29, v29, v249
	v_cvt_pk_bf16_f32 v29, v29, v228
	v_mul_f32_dpp v228, v30, v250 quad_perm:[1,0,3,2] row_mask:0xf bank_mask:0xf
	v_mul_f32_e32 v30, v30, v250
	v_cvt_pk_bf16_f32 v30, v30, v228
	v_mul_f32_dpp v228, v31, v251 quad_perm:[1,0,3,2] row_mask:0xf bank_mask:0xf
	v_mul_f32_e32 v31, v31, v251
	v_cvt_pk_bf16_f32 v31, v31, v228
	v_mul_f32_dpp v228, v32, v236 quad_perm:[1,0,3,2] row_mask:0xf bank_mask:0xf
	v_mul_f32_e32 v32, v32, v236
	v_cvt_pk_bf16_f32 v32, v32, v228
	v_mul_f32_dpp v228, v33, v237 quad_perm:[1,0,3,2] row_mask:0xf bank_mask:0xf
	v_mul_f32_e32 v33, v33, v237
	v_cvt_pk_bf16_f32 v33, v33, v228
	v_mul_f32_dpp v228, v34, v238 quad_perm:[1,0,3,2] row_mask:0xf bank_mask:0xf
	v_mul_f32_e32 v34, v34, v238
	v_cvt_pk_bf16_f32 v34, v34, v228
	v_mul_f32_dpp v228, v35, v239 quad_perm:[1,0,3,2] row_mask:0xf bank_mask:0xf
	v_mul_f32_e32 v35, v35, v239
	v_cvt_pk_bf16_f32 v35, v35, v228
	v_mul_f32_dpp v228, v36, v240 quad_perm:[1,0,3,2] row_mask:0xf bank_mask:0xf
	v_mul_f32_e32 v36, v36, v240
	v_cvt_pk_bf16_f32 v36, v36, v228
	v_mul_f32_dpp v228, v37, v241 quad_perm:[1,0,3,2] row_mask:0xf bank_mask:0xf
	v_mul_f32_e32 v37, v37, v241
	v_cvt_pk_bf16_f32 v37, v37, v228
	v_mul_f32_dpp v228, v38, v242 quad_perm:[1,0,3,2] row_mask:0xf bank_mask:0xf
	v_mul_f32_e32 v38, v38, v242
	v_cvt_pk_bf16_f32 v38, v38, v228
	v_mul_f32_dpp v228, v39, v243 quad_perm:[1,0,3,2] row_mask:0xf bank_mask:0xf
	v_mul_f32_e32 v39, v39, v243
	v_cvt_pk_bf16_f32 v39, v39, v228
	v_mul_f32_dpp v228, v40, v244 quad_perm:[1,0,3,2] row_mask:0xf bank_mask:0xf
	v_mul_f32_e32 v40, v40, v244
	v_cvt_pk_bf16_f32 v40, v40, v228
	v_mul_f32_dpp v228, v41, v245 quad_perm:[1,0,3,2] row_mask:0xf bank_mask:0xf
	v_mul_f32_e32 v41, v41, v245
	v_cvt_pk_bf16_f32 v41, v41, v228
	v_mul_f32_dpp v228, v42, v246 quad_perm:[1,0,3,2] row_mask:0xf bank_mask:0xf
	v_mul_f32_e32 v42, v42, v246
	v_cvt_pk_bf16_f32 v42, v42, v228
	v_mul_f32_dpp v228, v43, v247 quad_perm:[1,0,3,2] row_mask:0xf bank_mask:0xf
	v_mul_f32_e32 v43, v43, v247
	v_cvt_pk_bf16_f32 v43, v43, v228
	v_mul_f32_dpp v228, v44, v248 quad_perm:[1,0,3,2] row_mask:0xf bank_mask:0xf
	v_mul_f32_e32 v44, v44, v248
	v_cvt_pk_bf16_f32 v44, v44, v228
	v_mul_f32_dpp v228, v45, v249 quad_perm:[1,0,3,2] row_mask:0xf bank_mask:0xf
	v_mul_f32_e32 v45, v45, v249
	v_cvt_pk_bf16_f32 v45, v45, v228
	v_mul_f32_dpp v228, v46, v250 quad_perm:[1,0,3,2] row_mask:0xf bank_mask:0xf
	v_mul_f32_e32 v46, v46, v250
	v_cvt_pk_bf16_f32 v46, v46, v228
	v_mul_f32_dpp v228, v47, v251 quad_perm:[1,0,3,2] row_mask:0xf bank_mask:0xf
	v_mul_f32_e32 v47, v47, v251
	v_cvt_pk_bf16_f32 v47, v47, v228
	v_mul_f32_dpp v228, v48, v236 quad_perm:[1,0,3,2] row_mask:0xf bank_mask:0xf
	v_mul_f32_e32 v48, v48, v236
	v_cvt_pk_bf16_f32 v48, v48, v228
	v_mul_f32_dpp v228, v49, v237 quad_perm:[1,0,3,2] row_mask:0xf bank_mask:0xf
	v_mul_f32_e32 v49, v49, v237
	v_cvt_pk_bf16_f32 v49, v49, v228
	v_mul_f32_dpp v228, v50, v238 quad_perm:[1,0,3,2] row_mask:0xf bank_mask:0xf
	v_mul_f32_e32 v50, v50, v238
	v_cvt_pk_bf16_f32 v50, v50, v228
	v_mul_f32_dpp v228, v51, v239 quad_perm:[1,0,3,2] row_mask:0xf bank_mask:0xf
	v_mul_f32_e32 v51, v51, v239
	v_cvt_pk_bf16_f32 v51, v51, v228
	v_mul_f32_dpp v228, v52, v240 quad_perm:[1,0,3,2] row_mask:0xf bank_mask:0xf
	v_mul_f32_e32 v52, v52, v240
	v_cvt_pk_bf16_f32 v52, v52, v228
	v_mul_f32_dpp v228, v53, v241 quad_perm:[1,0,3,2] row_mask:0xf bank_mask:0xf
	v_mul_f32_e32 v53, v53, v241
	v_cvt_pk_bf16_f32 v53, v53, v228
	v_mul_f32_dpp v228, v54, v242 quad_perm:[1,0,3,2] row_mask:0xf bank_mask:0xf
	v_mul_f32_e32 v54, v54, v242
	v_cvt_pk_bf16_f32 v54, v54, v228
	v_mul_f32_dpp v228, v55, v243 quad_perm:[1,0,3,2] row_mask:0xf bank_mask:0xf
	v_mul_f32_e32 v55, v55, v243
	v_cvt_pk_bf16_f32 v55, v55, v228
	v_mul_f32_dpp v228, v56, v244 quad_perm:[1,0,3,2] row_mask:0xf bank_mask:0xf
	v_mul_f32_e32 v56, v56, v244
	v_cvt_pk_bf16_f32 v56, v56, v228
	v_mul_f32_dpp v228, v57, v245 quad_perm:[1,0,3,2] row_mask:0xf bank_mask:0xf
	v_mul_f32_e32 v57, v57, v245
	v_cvt_pk_bf16_f32 v57, v57, v228
	v_mul_f32_dpp v228, v58, v246 quad_perm:[1,0,3,2] row_mask:0xf bank_mask:0xf
	v_mul_f32_e32 v58, v58, v246
	v_cvt_pk_bf16_f32 v58, v58, v228
	v_mul_f32_dpp v228, v59, v247 quad_perm:[1,0,3,2] row_mask:0xf bank_mask:0xf
	v_mul_f32_e32 v59, v59, v247
	v_cvt_pk_bf16_f32 v59, v59, v228
	v_mul_f32_dpp v228, v60, v248 quad_perm:[1,0,3,2] row_mask:0xf bank_mask:0xf
	v_mul_f32_e32 v60, v60, v248
	v_cvt_pk_bf16_f32 v60, v60, v228
	v_mul_f32_dpp v228, v61, v249 quad_perm:[1,0,3,2] row_mask:0xf bank_mask:0xf
	v_mul_f32_e32 v61, v61, v249
	v_cvt_pk_bf16_f32 v61, v61, v228
	v_mul_f32_dpp v228, v62, v250 quad_perm:[1,0,3,2] row_mask:0xf bank_mask:0xf
	v_mul_f32_e32 v62, v62, v250
	v_cvt_pk_bf16_f32 v62, v62, v228
	v_mul_f32_dpp v228, v63, v251 quad_perm:[1,0,3,2] row_mask:0xf bank_mask:0xf
	v_mul_f32_e32 v63, v63, v251
	v_cvt_pk_bf16_f32 v63, v63, v228
	v_mul_f32_dpp v228, v64, v236 quad_perm:[1,0,3,2] row_mask:0xf bank_mask:0xf
	v_mul_f32_e32 v64, v64, v236
	v_cvt_pk_bf16_f32 v64, v64, v228
	v_mul_f32_dpp v228, v65, v237 quad_perm:[1,0,3,2] row_mask:0xf bank_mask:0xf
	v_mul_f32_e32 v65, v65, v237
	v_cvt_pk_bf16_f32 v65, v65, v228
	v_mul_f32_dpp v228, v66, v238 quad_perm:[1,0,3,2] row_mask:0xf bank_mask:0xf
	v_mul_f32_e32 v66, v66, v238
	v_cvt_pk_bf16_f32 v66, v66, v228
	v_mul_f32_dpp v228, v67, v239 quad_perm:[1,0,3,2] row_mask:0xf bank_mask:0xf
	v_mul_f32_e32 v67, v67, v239
	v_cvt_pk_bf16_f32 v67, v67, v228
	v_mul_f32_dpp v228, v68, v240 quad_perm:[1,0,3,2] row_mask:0xf bank_mask:0xf
	v_mul_f32_e32 v68, v68, v240
	v_cvt_pk_bf16_f32 v68, v68, v228
	v_mul_f32_dpp v228, v69, v241 quad_perm:[1,0,3,2] row_mask:0xf bank_mask:0xf
	v_mul_f32_e32 v69, v69, v241
	v_cvt_pk_bf16_f32 v69, v69, v228
	v_mul_f32_dpp v228, v70, v242 quad_perm:[1,0,3,2] row_mask:0xf bank_mask:0xf
	v_mul_f32_e32 v70, v70, v242
	v_cvt_pk_bf16_f32 v70, v70, v228
	v_mul_f32_dpp v228, v71, v243 quad_perm:[1,0,3,2] row_mask:0xf bank_mask:0xf
	v_mul_f32_e32 v71, v71, v243
	v_cvt_pk_bf16_f32 v71, v71, v228
	v_mul_f32_dpp v228, v72, v244 quad_perm:[1,0,3,2] row_mask:0xf bank_mask:0xf
	v_mul_f32_e32 v72, v72, v244
	v_cvt_pk_bf16_f32 v72, v72, v228
	v_mul_f32_dpp v228, v73, v245 quad_perm:[1,0,3,2] row_mask:0xf bank_mask:0xf
	v_mul_f32_e32 v73, v73, v245
	v_cvt_pk_bf16_f32 v73, v73, v228
	v_mul_f32_dpp v228, v74, v246 quad_perm:[1,0,3,2] row_mask:0xf bank_mask:0xf
	v_mul_f32_e32 v74, v74, v246
	v_cvt_pk_bf16_f32 v74, v74, v228
	v_mul_f32_dpp v228, v75, v247 quad_perm:[1,0,3,2] row_mask:0xf bank_mask:0xf
	v_mul_f32_e32 v75, v75, v247
	v_cvt_pk_bf16_f32 v75, v75, v228
	v_mul_f32_dpp v228, v76, v248 quad_perm:[1,0,3,2] row_mask:0xf bank_mask:0xf
	v_mul_f32_e32 v76, v76, v248
	v_cvt_pk_bf16_f32 v76, v76, v228
	v_mul_f32_dpp v228, v77, v249 quad_perm:[1,0,3,2] row_mask:0xf bank_mask:0xf
	v_mul_f32_e32 v77, v77, v249
	v_cvt_pk_bf16_f32 v77, v77, v228
	v_mul_f32_dpp v228, v78, v250 quad_perm:[1,0,3,2] row_mask:0xf bank_mask:0xf
	v_mul_f32_e32 v78, v78, v250
	v_cvt_pk_bf16_f32 v78, v78, v228
	v_mul_f32_dpp v228, v79, v251 quad_perm:[1,0,3,2] row_mask:0xf bank_mask:0xf
	v_mul_f32_e32 v79, v79, v251
	v_cvt_pk_bf16_f32 v79, v79, v228
	v_mul_f32_dpp v228, v80, v236 quad_perm:[1,0,3,2] row_mask:0xf bank_mask:0xf
	v_mul_f32_e32 v80, v80, v236
	v_cvt_pk_bf16_f32 v80, v80, v228
	v_mul_f32_dpp v228, v81, v237 quad_perm:[1,0,3,2] row_mask:0xf bank_mask:0xf
	v_mul_f32_e32 v81, v81, v237
	v_cvt_pk_bf16_f32 v81, v81, v228
	v_mul_f32_dpp v228, v82, v238 quad_perm:[1,0,3,2] row_mask:0xf bank_mask:0xf
	v_mul_f32_e32 v82, v82, v238
	v_cvt_pk_bf16_f32 v82, v82, v228
	v_mul_f32_dpp v228, v83, v239 quad_perm:[1,0,3,2] row_mask:0xf bank_mask:0xf
	v_mul_f32_e32 v83, v83, v239
	v_cvt_pk_bf16_f32 v83, v83, v228
	v_mul_f32_dpp v228, v84, v240 quad_perm:[1,0,3,2] row_mask:0xf bank_mask:0xf
	v_mul_f32_e32 v84, v84, v240
	v_cvt_pk_bf16_f32 v84, v84, v228
	v_mul_f32_dpp v228, v85, v241 quad_perm:[1,0,3,2] row_mask:0xf bank_mask:0xf
	v_mul_f32_e32 v85, v85, v241
	v_cvt_pk_bf16_f32 v85, v85, v228
	v_mul_f32_dpp v228, v86, v242 quad_perm:[1,0,3,2] row_mask:0xf bank_mask:0xf
	v_mul_f32_e32 v86, v86, v242
	v_cvt_pk_bf16_f32 v86, v86, v228
	v_mul_f32_dpp v228, v87, v243 quad_perm:[1,0,3,2] row_mask:0xf bank_mask:0xf
	v_mul_f32_e32 v87, v87, v243
	v_cvt_pk_bf16_f32 v87, v87, v228
	v_mul_f32_dpp v228, v88, v244 quad_perm:[1,0,3,2] row_mask:0xf bank_mask:0xf
	v_mul_f32_e32 v88, v88, v244
	v_cvt_pk_bf16_f32 v88, v88, v228
	v_mul_f32_dpp v228, v89, v245 quad_perm:[1,0,3,2] row_mask:0xf bank_mask:0xf
	v_mul_f32_e32 v89, v89, v245
	v_cvt_pk_bf16_f32 v89, v89, v228
	v_mul_f32_dpp v228, v90, v246 quad_perm:[1,0,3,2] row_mask:0xf bank_mask:0xf
	v_mul_f32_e32 v90, v90, v246
	v_cvt_pk_bf16_f32 v90, v90, v228
	v_mul_f32_dpp v228, v91, v247 quad_perm:[1,0,3,2] row_mask:0xf bank_mask:0xf
	v_mul_f32_e32 v91, v91, v247
	v_cvt_pk_bf16_f32 v91, v91, v228
	v_mul_f32_dpp v228, v92, v248 quad_perm:[1,0,3,2] row_mask:0xf bank_mask:0xf
	v_mul_f32_e32 v92, v92, v248
	v_cvt_pk_bf16_f32 v92, v92, v228
	v_mul_f32_dpp v228, v93, v249 quad_perm:[1,0,3,2] row_mask:0xf bank_mask:0xf
	v_mul_f32_e32 v93, v93, v249
	v_cvt_pk_bf16_f32 v93, v93, v228
	v_mul_f32_dpp v228, v94, v250 quad_perm:[1,0,3,2] row_mask:0xf bank_mask:0xf
	v_mul_f32_e32 v94, v94, v250
	v_cvt_pk_bf16_f32 v94, v94, v228
	v_mul_f32_dpp v228, v95, v251 quad_perm:[1,0,3,2] row_mask:0xf bank_mask:0xf
	v_mul_f32_e32 v95, v95, v251
	v_cvt_pk_bf16_f32 v95, v95, v228
	v_mul_f32_dpp v228, v98, v236 quad_perm:[1,0,3,2] row_mask:0xf bank_mask:0xf
	v_mul_f32_e32 v98, v98, v236
	v_cvt_pk_bf16_f32 v98, v98, v228
	v_mul_f32_dpp v228, v99, v237 quad_perm:[1,0,3,2] row_mask:0xf bank_mask:0xf
	v_mul_f32_e32 v99, v99, v237
	v_cvt_pk_bf16_f32 v99, v99, v228
	v_mul_f32_dpp v228, v100, v238 quad_perm:[1,0,3,2] row_mask:0xf bank_mask:0xf
	v_mul_f32_e32 v100, v100, v238
	v_cvt_pk_bf16_f32 v100, v100, v228
	v_mul_f32_dpp v228, v101, v239 quad_perm:[1,0,3,2] row_mask:0xf bank_mask:0xf
	v_mul_f32_e32 v101, v101, v239
	v_cvt_pk_bf16_f32 v101, v101, v228
	v_mul_f32_dpp v228, v102, v240 quad_perm:[1,0,3,2] row_mask:0xf bank_mask:0xf
	v_mul_f32_e32 v102, v102, v240
	v_cvt_pk_bf16_f32 v102, v102, v228
	v_mul_f32_dpp v228, v103, v241 quad_perm:[1,0,3,2] row_mask:0xf bank_mask:0xf
	v_mul_f32_e32 v103, v103, v241
	v_cvt_pk_bf16_f32 v103, v103, v228
	v_mul_f32_dpp v228, v104, v242 quad_perm:[1,0,3,2] row_mask:0xf bank_mask:0xf
	v_mul_f32_e32 v104, v104, v242
	v_cvt_pk_bf16_f32 v104, v104, v228
	v_mul_f32_dpp v228, v105, v243 quad_perm:[1,0,3,2] row_mask:0xf bank_mask:0xf
	v_mul_f32_e32 v105, v105, v243
	v_cvt_pk_bf16_f32 v105, v105, v228
	v_mul_f32_dpp v228, v106, v244 quad_perm:[1,0,3,2] row_mask:0xf bank_mask:0xf
	v_mul_f32_e32 v106, v106, v244
	v_cvt_pk_bf16_f32 v106, v106, v228
	v_mul_f32_dpp v228, v107, v245 quad_perm:[1,0,3,2] row_mask:0xf bank_mask:0xf
	v_mul_f32_e32 v107, v107, v245
	v_cvt_pk_bf16_f32 v107, v107, v228
	v_mul_f32_dpp v228, v108, v246 quad_perm:[1,0,3,2] row_mask:0xf bank_mask:0xf
	v_mul_f32_e32 v108, v108, v246
	v_cvt_pk_bf16_f32 v108, v108, v228
	v_mul_f32_dpp v228, v109, v247 quad_perm:[1,0,3,2] row_mask:0xf bank_mask:0xf
	v_mul_f32_e32 v109, v109, v247
	v_cvt_pk_bf16_f32 v109, v109, v228
	v_mul_f32_dpp v228, v110, v248 quad_perm:[1,0,3,2] row_mask:0xf bank_mask:0xf
	v_mul_f32_e32 v110, v110, v248
	v_cvt_pk_bf16_f32 v110, v110, v228
	v_mul_f32_dpp v228, v111, v249 quad_perm:[1,0,3,2] row_mask:0xf bank_mask:0xf
	v_mul_f32_e32 v111, v111, v249
	v_cvt_pk_bf16_f32 v111, v111, v228
	v_mul_f32_dpp v228, v112, v250 quad_perm:[1,0,3,2] row_mask:0xf bank_mask:0xf
	v_mul_f32_e32 v112, v112, v250
	v_cvt_pk_bf16_f32 v112, v112, v228
	v_mul_f32_dpp v228, v113, v251 quad_perm:[1,0,3,2] row_mask:0xf bank_mask:0xf
	v_mul_f32_e32 v113, v113, v251
	v_cvt_pk_bf16_f32 v113, v113, v228
	v_mul_f32_dpp v228, v114, v236 quad_perm:[1,0,3,2] row_mask:0xf bank_mask:0xf
	v_mul_f32_e32 v114, v114, v236
	v_cvt_pk_bf16_f32 v114, v114, v228
	v_mul_f32_dpp v228, v115, v237 quad_perm:[1,0,3,2] row_mask:0xf bank_mask:0xf
	v_mul_f32_e32 v115, v115, v237
	v_cvt_pk_bf16_f32 v115, v115, v228
	v_mul_f32_dpp v228, v116, v238 quad_perm:[1,0,3,2] row_mask:0xf bank_mask:0xf
	v_mul_f32_e32 v116, v116, v238
	v_cvt_pk_bf16_f32 v116, v116, v228
	v_mul_f32_dpp v228, v117, v239 quad_perm:[1,0,3,2] row_mask:0xf bank_mask:0xf
	v_mul_f32_e32 v117, v117, v239
	v_cvt_pk_bf16_f32 v117, v117, v228
	v_mul_f32_dpp v228, v118, v240 quad_perm:[1,0,3,2] row_mask:0xf bank_mask:0xf
	v_mul_f32_e32 v118, v118, v240
	v_cvt_pk_bf16_f32 v118, v118, v228
	v_mul_f32_dpp v228, v119, v241 quad_perm:[1,0,3,2] row_mask:0xf bank_mask:0xf
	v_mul_f32_e32 v119, v119, v241
	v_cvt_pk_bf16_f32 v119, v119, v228
	v_mul_f32_dpp v228, v120, v242 quad_perm:[1,0,3,2] row_mask:0xf bank_mask:0xf
	v_mul_f32_e32 v120, v120, v242
	v_cvt_pk_bf16_f32 v120, v120, v228
	v_mul_f32_dpp v228, v121, v243 quad_perm:[1,0,3,2] row_mask:0xf bank_mask:0xf
	v_mul_f32_e32 v121, v121, v243
	v_cvt_pk_bf16_f32 v121, v121, v228
	v_mul_f32_dpp v228, v122, v244 quad_perm:[1,0,3,2] row_mask:0xf bank_mask:0xf
	v_mul_f32_e32 v122, v122, v244
	v_cvt_pk_bf16_f32 v122, v122, v228
	v_mul_f32_dpp v228, v123, v245 quad_perm:[1,0,3,2] row_mask:0xf bank_mask:0xf
	v_mul_f32_e32 v123, v123, v245
	v_cvt_pk_bf16_f32 v123, v123, v228
	v_mul_f32_dpp v228, v124, v246 quad_perm:[1,0,3,2] row_mask:0xf bank_mask:0xf
	v_mul_f32_e32 v124, v124, v246
	v_cvt_pk_bf16_f32 v124, v124, v228
	v_mul_f32_dpp v228, v125, v247 quad_perm:[1,0,3,2] row_mask:0xf bank_mask:0xf
	v_mul_f32_e32 v125, v125, v247
	v_cvt_pk_bf16_f32 v125, v125, v228
	v_mul_f32_dpp v228, v126, v248 quad_perm:[1,0,3,2] row_mask:0xf bank_mask:0xf
	v_mul_f32_e32 v126, v126, v248
	v_cvt_pk_bf16_f32 v126, v126, v228
	v_mul_f32_dpp v228, v127, v249 quad_perm:[1,0,3,2] row_mask:0xf bank_mask:0xf
	v_mul_f32_e32 v127, v127, v249
	v_cvt_pk_bf16_f32 v127, v127, v228
	v_mul_f32_dpp v228, v128, v250 quad_perm:[1,0,3,2] row_mask:0xf bank_mask:0xf
	v_mul_f32_e32 v128, v128, v250
	v_cvt_pk_bf16_f32 v128, v128, v228
	v_mul_f32_dpp v228, v129, v251 quad_perm:[1,0,3,2] row_mask:0xf bank_mask:0xf
	v_mul_f32_e32 v129, v129, v251
	v_cvt_pk_bf16_f32 v129, v129, v228
	s_mov_b64 s[48:49], exec
	s_mov_b32 s50, 0x55555555
	s_mov_b32 s51, 0x55555555
	s_mov_b64 exec, s[50:51]
	global_store_dword v233, v0, s[42:43] offset:0
	global_store_dword v233, v1, s[42:43] offset:256
	global_store_dword v233, v2, s[42:43] offset:512
	global_store_dword v233, v3, s[42:43] offset:768
	global_store_dword v233, v4, s[42:43] offset:2048
	global_store_dword v233, v5, s[42:43] offset:2304
	global_store_dword v233, v6, s[42:43] offset:2560
	global_store_dword v233, v7, s[42:43] offset:2816
	global_store_dword v234, v8, s[42:43] offset:0
	global_store_dword v234, v9, s[42:43] offset:256
	global_store_dword v234, v10, s[42:43] offset:512
	global_store_dword v234, v11, s[42:43] offset:768
	global_store_dword v234, v12, s[42:43] offset:2048
	global_store_dword v234, v13, s[42:43] offset:2304
	global_store_dword v234, v14, s[42:43] offset:2560
	global_store_dword v234, v15, s[42:43] offset:2816
	global_store_dword v233, v16, s[42:43] offset:64
	global_store_dword v233, v17, s[42:43] offset:320
	global_store_dword v233, v18, s[42:43] offset:576
	global_store_dword v233, v19, s[42:43] offset:832
	global_store_dword v233, v20, s[42:43] offset:2112
	global_store_dword v233, v21, s[42:43] offset:2368
	global_store_dword v233, v22, s[42:43] offset:2624
	global_store_dword v233, v23, s[42:43] offset:2880
	global_store_dword v234, v24, s[42:43] offset:64
	global_store_dword v234, v25, s[42:43] offset:320
	global_store_dword v234, v26, s[42:43] offset:576
	global_store_dword v234, v27, s[42:43] offset:832
	global_store_dword v234, v28, s[42:43] offset:2112
	global_store_dword v234, v29, s[42:43] offset:2368
	global_store_dword v234, v30, s[42:43] offset:2624
	global_store_dword v234, v31, s[42:43] offset:2880
	global_store_dword v233, v32, s[42:43] offset:128
	global_store_dword v233, v33, s[42:43] offset:384
	global_store_dword v233, v34, s[42:43] offset:640
	global_store_dword v233, v35, s[42:43] offset:896
	global_store_dword v233, v36, s[42:43] offset:2176
	global_store_dword v233, v37, s[42:43] offset:2432
	global_store_dword v233, v38, s[42:43] offset:2688
	global_store_dword v233, v39, s[42:43] offset:2944
	global_store_dword v234, v40, s[42:43] offset:128
	global_store_dword v234, v41, s[42:43] offset:384
	global_store_dword v234, v42, s[42:43] offset:640
	global_store_dword v234, v43, s[42:43] offset:896
	global_store_dword v234, v44, s[42:43] offset:2176
	global_store_dword v234, v45, s[42:43] offset:2432
	global_store_dword v234, v46, s[42:43] offset:2688
	global_store_dword v234, v47, s[42:43] offset:2944
	global_store_dword v233, v48, s[42:43] offset:192
	global_store_dword v233, v49, s[42:43] offset:448
	global_store_dword v233, v50, s[42:43] offset:704
	global_store_dword v233, v51, s[42:43] offset:960
	global_store_dword v233, v52, s[42:43] offset:2240
	global_store_dword v233, v53, s[42:43] offset:2496
	global_store_dword v233, v54, s[42:43] offset:2752
	global_store_dword v233, v55, s[42:43] offset:3008
	global_store_dword v234, v56, s[42:43] offset:192
	global_store_dword v234, v57, s[42:43] offset:448
	global_store_dword v234, v58, s[42:43] offset:704
	global_store_dword v234, v59, s[42:43] offset:960
	global_store_dword v234, v60, s[42:43] offset:2240
	global_store_dword v234, v61, s[42:43] offset:2496
	global_store_dword v234, v62, s[42:43] offset:2752
	global_store_dword v234, v63, s[42:43] offset:3008
	global_store_dword v233, v64, s[44:45] offset:0
	global_store_dword v233, v65, s[44:45] offset:256
	global_store_dword v233, v66, s[44:45] offset:512
	global_store_dword v233, v67, s[44:45] offset:768
	global_store_dword v233, v68, s[44:45] offset:2048
	global_store_dword v233, v69, s[44:45] offset:2304
	global_store_dword v233, v70, s[44:45] offset:2560
	global_store_dword v233, v71, s[44:45] offset:2816
	global_store_dword v234, v72, s[44:45] offset:0
	global_store_dword v234, v73, s[44:45] offset:256
	global_store_dword v234, v74, s[44:45] offset:512
	global_store_dword v234, v75, s[44:45] offset:768
	global_store_dword v234, v76, s[44:45] offset:2048
	global_store_dword v234, v77, s[44:45] offset:2304
	global_store_dword v234, v78, s[44:45] offset:2560
	global_store_dword v234, v79, s[44:45] offset:2816
	global_store_dword v233, v80, s[44:45] offset:64
	global_store_dword v233, v81, s[44:45] offset:320
	global_store_dword v233, v82, s[44:45] offset:576
	global_store_dword v233, v83, s[44:45] offset:832
	global_store_dword v233, v84, s[44:45] offset:2112
	global_store_dword v233, v85, s[44:45] offset:2368
	global_store_dword v233, v86, s[44:45] offset:2624
	global_store_dword v233, v87, s[44:45] offset:2880
	global_store_dword v234, v88, s[44:45] offset:64
	global_store_dword v234, v89, s[44:45] offset:320
	global_store_dword v234, v90, s[44:45] offset:576
	global_store_dword v234, v91, s[44:45] offset:832
	global_store_dword v234, v92, s[44:45] offset:2112
	global_store_dword v234, v93, s[44:45] offset:2368
	global_store_dword v234, v94, s[44:45] offset:2624
	global_store_dword v234, v95, s[44:45] offset:2880
	global_store_dword v233, v98, s[44:45] offset:128
	global_store_dword v233, v99, s[44:45] offset:384
	global_store_dword v233, v100, s[44:45] offset:640
	global_store_dword v233, v101, s[44:45] offset:896
	global_store_dword v233, v102, s[44:45] offset:2176
	global_store_dword v233, v103, s[44:45] offset:2432
	global_store_dword v233, v104, s[44:45] offset:2688
	global_store_dword v233, v105, s[44:45] offset:2944
	global_store_dword v234, v106, s[44:45] offset:128
	global_store_dword v234, v107, s[44:45] offset:384
	global_store_dword v234, v108, s[44:45] offset:640
	global_store_dword v234, v109, s[44:45] offset:896
	global_store_dword v234, v110, s[44:45] offset:2176
	global_store_dword v234, v111, s[44:45] offset:2432
	global_store_dword v234, v112, s[44:45] offset:2688
	global_store_dword v234, v113, s[44:45] offset:2944
	global_store_dword v233, v114, s[44:45] offset:192
	global_store_dword v233, v115, s[44:45] offset:448
	global_store_dword v233, v116, s[44:45] offset:704
	global_store_dword v233, v117, s[44:45] offset:960
	global_store_dword v233, v118, s[44:45] offset:2240
	global_store_dword v233, v119, s[44:45] offset:2496
	global_store_dword v233, v120, s[44:45] offset:2752
	global_store_dword v233, v121, s[44:45] offset:3008
	global_store_dword v234, v122, s[44:45] offset:192
	global_store_dword v234, v123, s[44:45] offset:448
	global_store_dword v234, v124, s[44:45] offset:704
	global_store_dword v234, v125, s[44:45] offset:960
	global_store_dword v234, v126, s[44:45] offset:2240
	global_store_dword v234, v127, s[44:45] offset:2496
	global_store_dword v234, v128, s[44:45] offset:2752
	global_store_dword v234, v129, s[44:45] offset:3008
	s_mov_b64 exec, s[48:49]
	s_add_i32 s9, s9, 1
	s_cmp_lt_u32 s9, 4
	s_cbranch_scc1 .Lfa_block
	s_add_i32 s2, s2, s7
	s_branch .Lfa_task
